# attention near path: LUT addresses with pre-scaled base and bounds (2 VALU per element instead of 3)
# speedup vs baseline: 1.0131x; 1.0131x over previous
;     ...
;                 if (__any(qrel <= 64 * ck + 191)) {
; #pragma unroll
;                     for (int k2 = 0; k2 < 2; ++k2) {
;                         float bb[16];
; #pragma unroll
;                         for (int i = 0; i < 16; ++i) { const int key = 32 * (2 * ck + k2) + (i & 3) + 8 * (i >> 2) + 4 * half; const int n = qrel - key;
;                             bb[i] = LUT[1 + (n < -1 ? -1 : (n > 128 ? 128 : n))]; }
; #pragma unroll
;                         for (int i = 0; i < 16; ++i) asm volatile("" : "+v"(bb[i]));
; #pragma unroll
;                         for (int i = 0; i < 16; ++i) { const float s = sacc[k2][i] + bb[i]; sacc[k2][i] = s; mx = fmaxf(mx, s); } }
.LBB0_2230:
	v_mov_b32_e32 v64, v250
	s_waitcnt lgkmcnt(0)
	ds_read_b128 v[32:35], v251
	ds_read_b128 v[66:69], v251 offset:32
	ds_read_b128 v[70:73], v251 offset:64
	ds_read_b128 v[74:77], v251 offset:96
	ds_read_b128 v[78:81], v251 offset:4608
	ds_read_b128 v[122:125], v251 offset:4640
	v_cmp_ge_i32_e32 vcc, s22, v64
	s_waitcnt lgkmcnt(5)
	v_mfma_f32_32x32x16_bf16 v[48:63], v[32:35], v[110:113], 0
	s_waitcnt lgkmcnt(4)
	v_mfma_f32_32x32x16_bf16 v[48:63], v[66:69], v[106:109], v[48:63]
	ds_read_b128 v[66:69], v251 offset:4672
	s_waitcnt lgkmcnt(4)
	v_mfma_f32_32x32x16_bf16 v[48:63], v[70:73], v[102:105], v[48:63]
	ds_read_b128 v[70:73], v251 offset:4704
	s_waitcnt lgkmcnt(4)
	v_mfma_f32_32x32x16_bf16 v[48:63], v[74:77], v[98:101], v[48:63]
	s_waitcnt lgkmcnt(3)
	v_mfma_f32_32x32x16_bf16 v[32:47], v[78:81], v[110:113], 0
	s_waitcnt lgkmcnt(2)
	v_mfma_f32_32x32x16_bf16 v[32:47], v[122:125], v[106:109], v[32:47]
	s_waitcnt lgkmcnt(1)
	v_mfma_f32_32x32x16_bf16 v[32:47], v[66:69], v[102:105], v[32:47]
	s_waitcnt lgkmcnt(0)
	v_mfma_f32_32x32x16_bf16 v[32:47], v[70:73], v[98:101], v[32:47]
	s_cbranch_vccz .LBB0_2237
	v_add3_u32 v64, v155, v64, s21
	v_lshl_add_u32 v235, v64, 2, s33
	s_add_i32 s98, s33, -4
	v_lshl_add_u32 v234, v232, 2, s33
	v_subrev_u32_e32 v168, 172, v235
	v_subrev_u32_e32 v123, 4, v235
	v_subrev_u32_e32 v124, 8, v235
	v_subrev_u32_e32 v125, 12, v235
	v_subrev_u32_e32 v126, 32, v235
	v_subrev_u32_e32 v127, 36, v235
	v_subrev_u32_e32 v128, 40, v235
	v_subrev_u32_e32 v129, 44, v235
	v_subrev_u32_e32 v130, 64, v235
	v_subrev_u32_e32 v131, 68, v235
	v_subrev_u32_e32 v132, 72, v235
	v_subrev_u32_e32 v133, 76, v235
	v_subrev_u32_e32 v134, 96, v235
	v_subrev_u32_e32 v135, 100, v235
	v_subrev_u32_e32 v136, 104, v235
	v_subrev_u32_e32 v137, 108, v235
	v_med3_i32 v171, v168, s98, v234
	v_med3_i32 v122, v235, s98, v234
	v_med3_i32 v123, v123, s98, v234
	v_med3_i32 v124, v124, s98, v234
	v_med3_i32 v125, v125, s98, v234
	v_med3_i32 v126, v126, s98, v234
	v_med3_i32 v127, v127, s98, v234
	v_med3_i32 v128, v128, s98, v234
	v_med3_i32 v129, v129, s98, v234
	v_med3_i32 v130, v130, s98, v234
	v_med3_i32 v131, v131, s98, v234
	v_med3_i32 v132, v132, s98, v234
	v_med3_i32 v133, v133, s98, v234
	v_med3_i32 v134, v134, s98, v234
	v_med3_i32 v135, v135, s98, v234
	v_med3_i32 v136, v136, s98, v234
	v_med3_i32 v137, v137, s98, v234
	v_subrev_u32_e32 v168, 192, v235
	v_med3_i32 v172, v168, s98, v234
	ds_read_b32 v122, v122 offset:4
	ds_read_b32 v123, v123 offset:4
	ds_read_b32 v124, v124 offset:4
	ds_read_b32 v125, v125 offset:4
	ds_read_b32 v126, v126 offset:4
	ds_read_b32 v127, v127 offset:4
	ds_read_b32 v128, v128 offset:4
	ds_read_b32 v129, v129 offset:4
	ds_read_b32 v130, v130 offset:4
	ds_read_b32 v131, v131 offset:4
	ds_read_b32 v132, v132 offset:4
	ds_read_b32 v133, v133 offset:4
	ds_read_b32 v134, v134 offset:4
	ds_read_b32 v135, v135 offset:4
	ds_read_b32 v136, v136 offset:4
	ds_read_b32 v137, v137 offset:4
	v_subrev_u32_e32 v168, 196, v235
	s_waitcnt lgkmcnt(14)
	v_med3_i32 v173, v168, s98, v234
	s_waitcnt lgkmcnt(13)
	s_waitcnt lgkmcnt(12)
	v_pk_add_f32 v[122:123], v[48:49], v[122:123]
	v_subrev_u32_e32 v168, 200, v235
	s_waitcnt lgkmcnt(11)
	s_waitcnt lgkmcnt(10)
	v_max3_f32 v138, v122, s23, v123
	v_pk_add_f32 v[124:125], v[50:51], v[124:125]
	v_med3_i32 v174, v168, s98, v234
	s_waitcnt lgkmcnt(9)
	s_waitcnt lgkmcnt(8)
	v_max3_f32 v138, v138, v124, v125
	v_pk_add_f32 v[126:127], v[52:53], v[126:127]
	v_subrev_u32_e32 v168, 204, v235
	s_waitcnt lgkmcnt(7)
	s_waitcnt lgkmcnt(6)
	v_max3_f32 v138, v138, v126, v127
	v_pk_add_f32 v[128:129], v[54:55], v[128:129]
	v_med3_i32 v175, v168, s98, v234
	s_waitcnt lgkmcnt(5)
	s_waitcnt lgkmcnt(4)
	v_max3_f32 v138, v138, v128, v129
	v_pk_add_f32 v[130:131], v[56:57], v[130:131]
	v_subrev_u32_e32 v168, 224, v235
	s_waitcnt lgkmcnt(3)
	s_waitcnt lgkmcnt(2)
	v_max3_f32 v138, v138, v130, v131
	v_pk_add_f32 v[132:133], v[58:59], v[132:133]
	v_med3_i32 v203, v168, s98, v234
	s_waitcnt lgkmcnt(1)
	s_waitcnt lgkmcnt(0)
	v_max3_f32 v138, v138, v132, v133
	v_pk_add_f32 v[134:135], v[60:61], v[134:135]
	v_subrev_u32_e32 v168, 228, v235
	v_max3_f32 v138, v138, v134, v135
	v_pk_add_f32 v[136:137], v[62:63], v[136:137]
	v_med3_i32 v205, v168, s98, v234
	v_max3_f32 v166, v138, v136, v137
	v_subrev_u32_e32 v138, 128, v235
	v_subrev_u32_e32 v139, 132, v235
	v_subrev_u32_e32 v140, 136, v235
	v_subrev_u32_e32 v141, 140, v235
	v_subrev_u32_e32 v168, 232, v235
	v_med3_i32 v138, v138, s98, v234
	v_med3_i32 v139, v139, s98, v234
	v_med3_i32 v140, v140, s98, v234
	v_med3_i32 v141, v141, s98, v234
	v_subrev_u32_e32 v164, 160, v235
	v_subrev_u32_e32 v165, 164, v235
	v_subrev_u32_e32 v167, 168, v235
	v_med3_i32 v226, v168, s98, v234
	v_subrev_u32_e32 v64, 236, v235
	v_med3_i32 v164, v164, s98, v234
	v_med3_i32 v165, v165, s98, v234
	v_med3_i32 v167, v167, s98, v234
	v_med3_i32 v64, v64, s98, v234
	ds_read_b32 v138, v138 offset:4
	ds_read_b32 v139, v139 offset:4
	ds_read_b32 v140, v140 offset:4
	ds_read_b32 v141, v141 offset:4
	ds_read_b32 v168, v164 offset:4
	ds_read_b32 v169, v165 offset:4
	ds_read_b32 v170, v167 offset:4
	ds_read_b32 v171, v171 offset:4
	ds_read_b32 v172, v172 offset:4
	ds_read_b32 v173, v173 offset:4
	ds_read_b32 v174, v174 offset:4
	ds_read_b32 v175, v175 offset:4
	ds_read_b32 v204, v203 offset:4
	ds_read_b32 v205, v205 offset:4
	ds_read_b32 v226, v226 offset:4
	ds_read_b32 v227, v64 offset:4
	s_waitcnt lgkmcnt(14)
	s_waitcnt lgkmcnt(13)
	s_waitcnt lgkmcnt(12)
	s_waitcnt lgkmcnt(11)
	s_waitcnt lgkmcnt(10)
	s_waitcnt lgkmcnt(9)
	v_pk_add_f32 v[164:165], v[32:33], v[138:139]
	s_waitcnt lgkmcnt(8)
	v_pk_add_f32 v[168:169], v[36:37], v[168:169]
	v_max3_f32 v64, v166, v164, v165
	v_pk_add_f32 v[166:167], v[34:35], v[140:141]
	s_waitcnt lgkmcnt(7)
	s_waitcnt lgkmcnt(6)
	v_pk_add_f32 v[170:171], v[38:39], v[170:171]
	v_max3_f32 v64, v64, v166, v167
	v_max3_f32 v64, v64, v168, v169
	s_waitcnt lgkmcnt(5)
	s_waitcnt lgkmcnt(4)
	v_max3_f32 v64, v64, v170, v171
	v_pk_add_f32 v[172:173], v[40:41], v[172:173]
	v_pk_add_f32 v[174:175], v[42:43], v[174:175]
	v_max3_f32 v64, v64, v172, v173
	s_waitcnt lgkmcnt(3)
	s_waitcnt lgkmcnt(2)
	v_max3_f32 v64, v64, v174, v175
	v_pk_add_f32 v[138:139], v[44:45], v[204:205]
	s_waitcnt lgkmcnt(1)
	s_waitcnt lgkmcnt(0)
	v_max3_f32 v64, v64, v138, v139
	v_pk_add_f32 v[140:141], v[46:47], v[226:227]
	s_nop 0
	v_max3_f32 v64, v64, v140, v141
	s_cbranch_execnz .LBB0_2233
